# v35 + neighbourhood attention: the 32 per-tile bias LDS reads pipelined 15 deep (were issued one or two at a time with a wait after each)
# speedup vs baseline: 1.0001x; 1.0001x over previous
.LBB0_716:
	s_andn2_b64 vcc, exec, vcc
	s_cbranch_vccnz .LBB0_718
	s_waitcnt lgkmcnt(0)
	v_add_u32_e32 v166, s87, v207
	ds_read_b32 v166, v166 offset:1536
	v_add_u32_e32 v167, s87, v206
	ds_read_b32 v167, v167 offset:1536
	v_add_u32_e32 v208, s87, v204
	ds_read_b32 v208, v208 offset:1536
	v_add_u32_e32 v209, s87, v205
	ds_read_b32 v209, v209 offset:1536
	v_add_u32_e32 v210, s87, v203
	ds_read_b32 v210, v210 offset:1536
	v_add_u32_e32 v211, s87, v202
	ds_read_b32 v211, v211 offset:1536
	v_add_u32_e32 v214, s87, v201
	ds_read_b32 v214, v214 offset:1536
	v_add_u32_e32 v215, s87, v200
	ds_read_b32 v215, v215 offset:1536
	v_add_u32_e32 v216, s87, v198
	ds_read_b32 v216, v216 offset:1536
	v_add_u32_e32 v217, s87, v199
	ds_read_b32 v217, v217 offset:1536
	v_add_u32_e32 v218, s87, v197
	ds_read_b32 v218, v218 offset:1536
	v_add_u32_e32 v220, s87, v196
	ds_read_b32 v220, v220 offset:1536
	v_add_u32_e32 v221, s87, v194
	ds_read_b32 v221, v221 offset:1536
	v_add_u32_e32 v222, s87, v195
	ds_read_b32 v222, v222 offset:1536
	v_add_u32_e32 v223, s87, v193
	ds_read_b32 v223, v223 offset:1536
	v_add_u32_e32 v116, s87, v207
	s_waitcnt lgkmcnt(14)
	v_mov_b32_e32 v116, v166
	v_add_u32_e32 v166, s87, v192
	ds_read_b32 v166, v166 offset:1536
	v_add_u32_e32 v117, s87, v206
	s_waitcnt lgkmcnt(14)
	v_mov_b32_e32 v117, v167
	v_add_u32_e32 v167, s87, v191
	ds_read_b32 v167, v167 offset:1536
	s_nop 1
	v_fmac_f32_e32 v116, 0x3e38aa3b, v48
	v_add_u32_e32 v48, s87, v204
	s_waitcnt lgkmcnt(14)
	v_mov_b32_e32 v48, v208
	v_add_u32_e32 v208, s87, v190
	ds_read_b32 v208, v208 offset:1536
	v_fmac_f32_e32 v117, 0x3e38aa3b, v32
	v_add_u32_e32 v32, s87, v205
	s_waitcnt lgkmcnt(14)
	v_mov_b32_e32 v32, v209
	v_add_u32_e32 v209, s87, v189
	ds_read_b32 v209, v209 offset:1536
	v_cndmask_b32_e64 v118, v219, v117, s[10:11]
	v_fmac_f32_e32 v48, 0x3e38aa3b, v33
	v_add_u32_e32 v33, s87, v203
	s_waitcnt lgkmcnt(14)
	v_mov_b32_e32 v33, v210
	v_add_u32_e32 v210, s87, v188
	ds_read_b32 v210, v210 offset:1536
	v_cndmask_b32_e64 v119, v219, v48, s[12:13]
	v_add_u32_e32 v48, s87, v202
	s_waitcnt lgkmcnt(14)
	v_mov_b32_e32 v121, v211
	v_add_u32_e32 v211, s87, v187
	ds_read_b32 v211, v211 offset:1536
	v_mov_b32_e32 v48, v49
	v_mov_b32_e32 v49, v50
	v_pk_fma_f32 v[32:33], v[48:49], s[90:91], v[32:33] op_sel_hi:[1,0,1]
	v_cndmask_b32_e64 v116, v116, v219, s[8:9]
	v_cndmask_b32_e64 v117, v32, v219, s[16:17]
	v_cndmask_b32_e64 v120, v33, v219, s[14:15]
	v_add_u32_e32 v32, s87, v201
	v_add_u32_e32 v33, s87, v200
	s_waitcnt lgkmcnt(14)
	v_mov_b32_e32 v32, v214
	v_add_u32_e32 v214, s87, v186
	ds_read_b32 v214, v214 offset:1536
	s_waitcnt lgkmcnt(14)
	v_mov_b32_e32 v33, v215
	v_add_u32_e32 v215, s87, v185
	ds_read_b32 v215, v215 offset:1536
	v_fmac_f32_e32 v121, 0x3e38aa3b, v34
	v_add_u32_e32 v34, s87, v198
	s_waitcnt lgkmcnt(14)
	v_mov_b32_e32 v48, v216
	v_add_u32_e32 v216, s87, v184
	ds_read_b32 v216, v216 offset:1536
	v_mov_b32_e32 v34, v51
	v_fmac_f32_e32 v33, 0x3e38aa3b, v35
	v_cndmask_b32_e64 v123, v219, v33, s[20:21]
	v_add_u32_e32 v33, s87, v199
	s_waitcnt lgkmcnt(14)
	v_mov_b32_e32 v33, v217
	v_add_u32_e32 v217, s87, v183
	ds_read_b32 v217, v217 offset:1536
	v_mov_b32_e32 v35, v52
	v_cndmask_b32_e64 v122, v219, v121, s[18:19]
	v_fmac_f32_e32 v48, 0x3e38aa3b, v36
	v_cndmask_b32_e64 v126, v219, v48, s[26:27]
	v_pk_fma_f32 v[32:33], v[34:35], s[90:91], v[32:33] op_sel_hi:[1,0,1]
	v_add_u32_e32 v34, s87, v194
	v_cndmask_b32_e64 v121, v32, v219, s[24:25]
	v_cndmask_b32_e64 v124, v33, v219, s[22:23]
	v_add_u32_e32 v32, s87, v197
	v_add_u32_e32 v33, s87, v196
	s_waitcnt lgkmcnt(14)
	v_mov_b32_e32 v32, v218
	v_add_u32_e32 v218, s87, v182
	ds_read_b32 v218, v218 offset:1536
	s_waitcnt lgkmcnt(14)
	v_mov_b32_e32 v33, v220
	v_add_u32_e32 v220, s87, v181
	ds_read_b32 v220, v220 offset:1536
	s_waitcnt lgkmcnt(14)
	v_mov_b32_e32 v36, v221
	v_add_u32_e32 v221, s87, v180
	ds_read_b32 v221, v221 offset:1536
	v_mov_b32_e32 v34, v53
	v_mov_b32_e32 v35, v54
	v_fmac_f32_e32 v33, 0x3e38aa3b, v37
	v_cndmask_b32_e64 v127, v219, v33, s[28:29]
	v_add_u32_e32 v33, s87, v195
	s_waitcnt lgkmcnt(14)
	v_mov_b32_e32 v33, v222
	v_add_u32_e32 v222, s87, v179
	ds_read_b32 v222, v222 offset:1536
	v_fmac_f32_e32 v36, 0x3e38aa3b, v38
	v_cndmask_b32_e64 v130, v219, v36, s[36:37]
	v_pk_fma_f32 v[32:33], v[34:35], s[90:91], v[32:33] op_sel_hi:[1,0,1]
	s_nop 0
	v_cndmask_b32_e64 v125, v32, v219, s[34:35]
	v_add_u32_e32 v32, s87, v193
	v_cndmask_b32_e64 v128, v33, v219, s[30:31]
	s_waitcnt lgkmcnt(14)
	v_mov_b32_e32 v32, v223
	v_add_u32_e32 v223, s87, v178
	ds_read_b32 v223, v223 offset:1536
	v_add_u32_e32 v33, s87, v192
	s_waitcnt lgkmcnt(14)
	v_mov_b32_e32 v33, v166
	v_add_u32_e32 v166, s87, v177
	ds_read_b32 v166, v166 offset:1536
	v_fmac_f32_e32 v32, 0x3e38aa3b, v55
	v_cndmask_b32_e64 v129, v32, v219, s[38:39]
	v_fmac_f32_e32 v33, 0x3e38aa3b, v39
	v_add_u32_e32 v32, s87, v191
	v_cndmask_b32_e64 v131, v219, v33, s[40:41]
	s_waitcnt lgkmcnt(14)
	v_mov_b32_e32 v33, v167
	v_add_u32_e32 v167, s87, v176
	ds_read_b32 v167, v167 offset:1536
	v_add_u32_e32 v32, s87, v190
	s_waitcnt lgkmcnt(14)
	v_mov_b32_e32 v32, v208
	v_fmac_f32_e32 v33, 0x3e38aa3b, v56
	v_cndmask_b32_e64 v132, v219, v33, s[42:43]
	v_add_u32_e32 v33, s87, v189
	s_waitcnt lgkmcnt(13)
	v_mov_b32_e32 v34, v209
	v_add_u32_e32 v33, s87, v188
	s_waitcnt lgkmcnt(12)
	v_mov_b32_e32 v33, v210
	v_fmac_f32_e32 v34, 0x3e38aa3b, v57
	v_cndmask_b32_e64 v133, v219, v34, s[44:45]
	v_pk_fma_f32 v[32:33], v[40:41], s[90:91], v[32:33] op_sel_hi:[1,0,1]
	s_nop 0
	v_cndmask_b32_e64 v136, v219, v32, s[48:49]
	v_add_u32_e32 v32, s87, v187
	v_cndmask_b32_e64 v137, v219, v33, s[46:47]
	s_waitcnt lgkmcnt(11)
	v_mov_b32_e32 v33, v211
	v_add_u32_e32 v32, s87, v186
	s_waitcnt lgkmcnt(10)
	v_mov_b32_e32 v32, v214
	v_fmac_f32_e32 v33, 0x3e38aa3b, v58
	v_cndmask_b32_e64 v134, v219, v33, s[50:51]
	v_add_u32_e32 v33, s87, v185
	s_waitcnt lgkmcnt(9)
	v_mov_b32_e32 v34, v215
	v_add_u32_e32 v33, s87, v184
	s_waitcnt lgkmcnt(8)
	v_mov_b32_e32 v33, v216
	v_fmac_f32_e32 v34, 0x3e38aa3b, v59
	v_cndmask_b32_e64 v135, v219, v34, s[52:53]
	v_pk_fma_f32 v[32:33], v[42:43], s[90:91], v[32:33] op_sel_hi:[1,0,1]
	s_nop 0
	v_cndmask_b32_e64 v142, v219, v32, s[56:57]
	v_add_u32_e32 v32, s87, v183
	v_cndmask_b32_e64 v143, v219, v33, s[54:55]
	s_waitcnt lgkmcnt(7)
	v_mov_b32_e32 v33, v217
	v_add_u32_e32 v32, s87, v182
	s_waitcnt lgkmcnt(6)
	v_mov_b32_e32 v32, v218
	v_fmac_f32_e32 v33, 0x3e38aa3b, v60
	v_cndmask_b32_e64 v138, v219, v33, s[58:59]
	v_add_u32_e32 v33, s87, v181
	s_waitcnt lgkmcnt(5)
	v_mov_b32_e32 v34, v220
	v_add_u32_e32 v33, s87, v180
	s_waitcnt lgkmcnt(4)
	v_mov_b32_e32 v33, v221
	v_fmac_f32_e32 v34, 0x3e38aa3b, v61
	v_cndmask_b32_e64 v139, v219, v34, s[60:61]
	v_pk_fma_f32 v[32:33], v[44:45], s[90:91], v[32:33] op_sel_hi:[1,0,1]
	s_nop 0
	v_cndmask_b32_e64 v144, v219, v32, s[64:65]
	v_add_u32_e32 v32, s87, v179
	v_cndmask_b32_e64 v145, v219, v33, s[62:63]
	s_waitcnt lgkmcnt(3)
	v_mov_b32_e32 v33, v222
	v_add_u32_e32 v32, s87, v178
	s_waitcnt lgkmcnt(2)
	v_mov_b32_e32 v32, v223
	v_fmac_f32_e32 v33, 0x3e38aa3b, v62
	v_cndmask_b32_e64 v140, v219, v33, s[66:67]
	v_add_u32_e32 v33, s87, v177
	s_waitcnt lgkmcnt(1)
	v_mov_b32_e32 v34, v166
	v_add_u32_e32 v33, s87, v176
	s_waitcnt lgkmcnt(0)
	v_mov_b32_e32 v33, v167
	v_fmac_f32_e32 v34, 0x3e38aa3b, v63
	v_cndmask_b32_e64 v141, v219, v34, s[68:69]
	v_pk_fma_f32 v[32:33], v[46:47], s[90:91], v[32:33] op_sel_hi:[1,0,1]
	s_nop 0
	v_cndmask_b32_e64 v146, v219, v32, s[72:73]
	v_cndmask_b32_e64 v147, v219, v33, s[70:71]
